# ILC6-nt with 18 slots in the diff loop and 31 in the MLA loop in strict wave-group alternation (no back-to-back converter iterations)
# speedup vs baseline: 1.0131x; 1.0131x over previous
; #define VM_WAIT() asm volatile("s_waitcnt vmcnt(0)" ::: "memory")
; #define SBAR() __builtin_amdgcn_sched_barrier(0)
; #define RESC(a) do { if (__any((a) < 1.f)) { if (hi == 0) al_l[r32] = (a); asm volatile("s_waitcnt lgkmcnt(0)" ::: "memory"); \
;         _Pragma("unroll") for (int d = 0; d < 4; ++d) _Pragma("unroll") for (int r = 0; r < 16; ++r) o[d][r] *= al_l[crow(r, hi)]; } } while (0)
;     ...
;         f32x16 pB0, pB1; float mnB, alB;
;         GLDS3(0); GLDS3(1); VM_WAIT(); __syncthreads();
;         qkt<MODE>(p0, p1, KB3(0), qr, r32, hi); partialSM<MODE>(p0, p1, m_reg, mn, al);
; #pragma unroll 1
;         for (int j = 1; j + 1 < NT; j += 2) {
;             GLDS3(j + 1);
;             SBAR(); qkt<MODE>(pB0, pB1, KB3(j), qr, r32, hi);
;             finishSM(p0, p1, al, l_reg, pa0, pa1, pa2, pa3); SBAR();
;             pv_d0(o, VB3(j - 1), pa0, pa1, pa2, pa3); partialSM<MODE>(pB0, pB1, m_reg, mnB, alB);
;             RESC(alB); VM_WAIT(); __syncthreads();
;             if (j + 2 < NT) GLDS3(j + 2);
.LBB0_487:
	s_mul_i32 s0, s18, 0xab
	s_addk_i32 s0, 0x201
	s_bfe_u32 s0, s0, 0x70009
	s_mul_i32 s0, s0, 3
	s_sub_i32 s0, s18, s0
	s_add_i32 s0, s0, 3
	s_and_b32 s0, s0, 0xff
	s_lshl_b32 s1, s0, 14
	s_mulk_i32 s0, 0x6000
	s_add_i32 s1, s14, s1
	s_add_i32 s17, s0, 0
	v_lshl_add_u64 v[118:119], s[6:7], 0, v[114:115]
	s_add_i32 s0, s17, s13
	v_lshl_add_u64 v[64:65], v[118:119], 0, s[22:23]
	s_mov_b32 m0, s1
	v_lshl_add_u64 v[120:121], s[6:7], 0, v[116:117]
	s_add_i32 s4, s0, 0xc000
	global_load_lds_dwordx4 v[64:65], off
	v_lshl_add_u64 v[64:65], v[120:121], 0, s[22:23]
	s_add_i32 m0, s1, 0x2000
	v_lshl_add_u64 v[122:123], s[6:7], 0, v[192:193]
	s_mov_b64 s[0:1], 0x2901880
	global_load_lds_dwordx4 v[64:65], off
	v_lshl_add_u64 v[64:65], v[122:123], 0, s[0:1]
	s_mov_b32 m0, s4
	s_add_i32 s15, s18, 2
	global_load_lds_dwordx4 v[64:65], off
	s_add_u32 s52, s52, 18
	s_cmp_ge_u32 s52, 31
	s_cselect_b32 s50, 1, 0
	s_cbranch_scc0 .Lilc_n_da
	s_sub_u32 s52, s52, 31
	s_mov_b32 s46, s51
	s_add_u32 s51, s51, 1
	s_lshl_b32 s49, s46, 2
	s_add_u32 s49, s49, s54
	s_cmp_lt_u32 s49, 0xc3
	s_cselect_b32 s50, 1, 0
	s_cbranch_scc0 .Lilc_n_da
	s_lshr_b32 s55, s46, 4
	s_and_b32 s57, s49, 63
	s_lshl_b32 s101, s56, 6
	s_add_u32 s101, s101, s57
	s_cmp_eq_u32 s55, 3
	s_cselect_b32 s55, s54, s55
	s_cselect_b32 s100, 3, 0
	s_cselect_b32 s101, s56, s101
	s_cselect_b32 s57, 64, s57
	s_add_u32 s100, s100, s55
	s_lshl_b32 s100, s100, 3
	s_add_u32 s100, s100, 0xa0
	s_load_dwordx2 s[44:45], s[36:37], s100

; #define VM_WAIT() asm volatile("s_waitcnt vmcnt(0)" ::: "memory")
; #define SBAR() __builtin_amdgcn_sched_barrier(0)
; #define RESC(a) do { if (__any((a) < 1.f)) { if (hi == 0) al_l[r32] = (a); asm volatile("s_waitcnt lgkmcnt(0)" ::: "memory"); \
;         _Pragma("unroll") for (int d = 0; d < 4; ++d) _Pragma("unroll") for (int r = 0; r < 16; ++r) o[d][r] *= al_l[crow(r, hi)]; } } while (0)
;     ...
;         f32x16 pB0, pB1; float mnB, alB;
;         GLDS3(0); GLDS3(1); VM_WAIT(); __syncthreads();
;         qkt<MODE>(p0, p1, KB3(0), qr, r32, hi); partialSM<MODE>(p0, p1, m_reg, mn, al);
; #pragma unroll 1
;         for (int j = 1; j + 1 < NT; j += 2) {
;             GLDS3(j + 1);
;             SBAR(); qkt<MODE>(pB0, pB1, KB3(j), qr, r32, hi);
;             finishSM(p0, p1, al, l_reg, pa0, pa1, pa2, pa3); SBAR();
;             pv_d0(o, VB3(j - 1), pa0, pa1, pa2, pa3); partialSM<MODE>(pB0, pB1, m_reg, mnB, alB);
;             RESC(alB); VM_WAIT(); __syncthreads();
;             if (j + 2 < NT) GLDS3(j + 2);
.LBB0_499:
	s_mul_i32 s0, s16, 0xab
	s_addk_i32 s0, 0x201
	s_bfe_u32 s0, s0, 0x70009
	s_mul_i32 s0, s0, 3
	s_sub_i32 s0, s16, s0
	s_add_i32 s0, s0, 3
	s_and_b32 s0, s0, 0xff
	s_lshl_b32 s1, s0, 14
	s_mulk_i32 s0, 0x6000
	s_add_i32 s1, s12, s1
	s_add_i32 s15, s0, 0
	v_lshl_add_u64 v[118:119], s[6:7], 0, v[114:115]
	s_add_i32 s0, s15, s11
	v_lshl_add_u64 v[64:65], v[118:119], 0, s[20:21]
	s_mov_b32 m0, s1
	v_lshl_add_u64 v[120:121], s[6:7], 0, v[116:117]
	s_add_i32 s4, s0, 0xc000
	global_load_lds_dwordx4 v[64:65], off
	v_lshl_add_u64 v[64:65], v[120:121], 0, s[20:21]
	s_add_i32 m0, s1, 0x2000
	v_lshl_add_u64 v[122:123], s[6:7], 0, v[192:193]
	s_mov_b64 s[0:1], 0x2901800
	global_load_lds_dwordx4 v[64:65], off
	v_lshl_add_u64 v[64:65], v[122:123], 0, s[0:1]
	s_mov_b32 m0, s4
	s_add_i32 s13, s16, 2
	global_load_lds_dwordx4 v[64:65], off
	s_add_u32 s52, s52, 18
	s_cmp_ge_u32 s52, 31
	s_cselect_b32 s50, 1, 0
	s_cbranch_scc0 .Lilc_n_db
	s_sub_u32 s52, s52, 31
	s_mov_b32 s46, s51
	s_add_u32 s51, s51, 1
	s_lshl_b32 s49, s46, 2
	s_add_u32 s49, s49, s54
	s_cmp_lt_u32 s49, 0xc3
	s_cselect_b32 s50, 1, 0
	s_cbranch_scc0 .Lilc_n_db
	s_lshr_b32 s55, s46, 4
	s_and_b32 s57, s49, 63
	s_lshl_b32 s101, s56, 6
	s_add_u32 s101, s101, s57
	s_cmp_eq_u32 s55, 3
	s_cselect_b32 s55, s54, s55
	s_cselect_b32 s100, 3, 0
	s_cselect_b32 s101, s56, s101
	s_cselect_b32 s57, 64, s57
	s_add_u32 s100, s100, s55
	s_lshl_b32 s100, s100, 3
	s_add_u32 s100, s100, 0xa0
	s_load_dwordx2 s[44:45], s[36:37], s100

;     ...
;     int tid = tid_x(); asm volatile("" : "+v"(tid));
;     const int wid = tid >> 6, lane = tid & 63, r32 = lane & 31, hi = lane >> 5;
;     const int qb = uid & 15, h = (uid >> 4) % NH, b = (uid >> 4) / NH;
;     const int tok0 = b * SEQ;
;     const int qrow = tok0 + qb * 256 + wid * 32 + r32;
;     LAS char* V_lds = lds + LDS_VBUF; LAS char* K_lds = lds + LDS_KBUF;
;     LAS float* ws = (LAS float*)(lds + LDS_WS) + wid * 64; LAS float* li_l = ws; LAS float* al_l = ws + 32;
;     LAS float* rpbL = (LAS float*)(lds + LDS_RPB);
;     const int sr = tid >> 4, sc = (tid & 15) * 8, vst0 = v_st(sr, sc), vst1 = v_st(32 + sr, sc);
;     const int sr64 = tid >> 3, sc64 = (tid & 7) * 8;
;     const int vb0 = (int)(unsigned)(uintptr_t)V_lds + v_rd_base(lane);
;     int NT = 64, kbase = tok0;
;     int rq = 0, qc = 0, kr_lo = 0;
;     if constexpr (MODE == MODE_NA) { const int rq0 = qb * 4; kr_lo = min(min(max(rq0 - 4, 0), 56), 52); NT = 12; kbase = tok0 + kr_lo * 64; rq = rq0 + (wid >> 1); qc = (wid & 1) * 32 + r32;
;         for (int i = tid; i < 15 * 31; i += 512) rpbL[i] = P.rpb[h * 465 + i];
;         __syncthreads(); }
;     const bf16* Kg; const bf16* Vg; const bf16* Kg2 = nullptr; int ldk, ldv;
;     if constexpr (MODE == MODE_MLA) { Kg = P.KVM + h * 256; Vg = P.KVM + h * 256 + 128; Kg2 = P.U + U_KR; ldk = KVW; ldv = KVW; }
;     else if constexpr (MODE == MODE_NA) { Kg = P.U + U_NA + 512 + h * 128; Vg = P.U + U_NA + 1024 + h * 128; ldk = UW; ldv = UW; }
;     else { Kg = P.U + U_DF + 512 + h * 128; Vg = P.U + U_DF + 1024 + h * 128; ldk = UW; ldv = UW; }
;     constexpr int pass = PASS;
;     constexpr bool HALF_OFFSET = false;
;     {
;         float m_reg = -1e30f, l_reg = 0; f32x16 o[4] = {}; bf16x8 qr[NQ];
;         if constexpr (MODE == MODE_MLA) {
;             const bf16* Qw = P.QM + (size_t)qrow * QMW + h * 192 + hi * 8;
; #pragma unroll
;             for (int d0 = 0; d0 < 12; ++d0) qr[d0] = *(const bf16x8*)(Qw + d0 * 16);
;             const f32x2* rt = P.ropeM + (size_t)(qrow & (SEQ - 1)) * 32;
; #pragma unroll
;             for (int g = 0; g < 2; ++g) {
;                 bf16x8 x1 = qr[8 + g], x2 = qr[10 + g];
; #pragma unroll
;                 for (int e = 0; e < 8; ++e) { const f32x2 cs = rt[g * 16 + hi * 8 + e];
;                     const float a = bf2f((unsigned short)x1[e]), c = bf2f((unsigned short)x2[e]);
.LBB0_785:
	s_lshl_b32 s0, s22, 1
	s_and_b32 s0, s0, 14
	s_ashr_i32 s1, s22, 7
	s_add_i32 s0, s0, s1
	s_getreg_b32 s1, hwreg(HW_REG_HW_ID, 0, 6)
	s_and_b32 s1, s1, 63
	s_lshl_b32 s1, s1, 2
	s_add_i32 s1, s1, 0
	s_add_i32 s1, s1, 0x23f00
	s_waitcnt vmcnt(15)
	v_mov_b32_e32 v0, s1
	ds_read_b32 v0, v0
	v_mbcnt_lo_u32_b32 v1, -1, 0
	v_mbcnt_hi_u32_b32 v1, -1, v1
	v_mov_b32_e32 v145, v193
	v_mov_b32_e32 v149, v193
	s_movk_i32 s3, 0x70
	s_waitcnt lgkmcnt(0)
	v_readfirstlane_b32 s1, v0
	s_mov_b32 s28, 0
	s_and_b32 s39, s74, 63
	s_lshl_b32 s39, s39, 3
	s_add_u32 s39, s39, s1
	s_lshr_b32 s54, s74, 6
	v_lshrrev_b32_e32 v226, 3, v1
	v_and_b32_e32 v229, 7, v1
	v_readlane_b32 s56, v254, 60
	s_lshr_b32 s52, s1, 2
	s_mul_i32 s52, s52, -31
	s_add_i32 s52, s52, 31
	s_mov_b32 s42, 0
	s_mov_b32 s51, 18
	s_mov_b32 s53, 0
	v_mov_b32_e32 v147, v193
	s_waitcnt vmcnt(13)
	v_lshl_add_u32 v11, s1, 6, v1
	s_lshr_b32 s1, s0, 29
	s_add_i32 s1, s0, s1
	s_and_b32 s2, s1, -8
	s_sub_i32 s23, s0, s2
	s_lshl_b32 s0, s1, 9
	s_and_b32 s4, s0, 0xfffff000
	s_lshl_b32 s0, s22, 5
	s_and_b32 s0, s0, 0xf00
	s_or_b32 s25, s4, s0
	v_ashrrev_i32_e32 v156, 6, v11
	v_and_b32_e32 v154, 31, v11
	v_lshl_add_u32 v0, v156, 5, s25
	v_or_b32_e32 v8, v0, v154
	v_and_b32_e32 v0, 0x3fffffc0, v11
	s_add_i32 s0, 0, 0x1e000
	v_lshl_add_u32 v157, v0, 2, s0
	s_lshl_b32 s0, s23, 8
	s_ashr_i32 s1, s0, 31
	s_lshl_b64 s[0:1], s[0:1], 1
	s_add_u32 s26, s18, s0
	v_mov_b64_e32 v[0:1], s[10:11]
	s_movk_i32 s0, 0xc00
	s_addc_u32 s27, s19, s1
	v_mad_i64_i32 v[0:1], s[0:1], v8, s0, v[0:1]
	s_mul_i32 s0, s23, 0xc0
	v_lshlrev_b32_e32 v8, 8, v8
	v_bfe_u32 v155, v11, 5, 1
	s_ashr_i32 s1, s0, 31
	v_and_b32_e32 v192, 0xfff00, v8
	v_lshl_add_u64 v[0:1], s[0:1], 1, v[0:1]
	v_lshlrev_b32_e32 v144, 4, v155
	v_lshl_add_u64 v[8:9], s[12:13], 0, v[192:193]
	v_lshlrev_b32_e32 v192, 6, v155
	v_lshl_add_u64 v[4:5], v[0:1], 0, v[144:145]
	v_lshl_add_u64 v[8:9], v[8:9], 0, v[192:193]
	global_load_dwordx4 v[96:99], v[4:5], off
	global_load_dwordx4 v[100:103], v[4:5], off offset:32
	global_load_dwordx4 v[104:107], v[4:5], off offset:64
	global_load_dwordx4 v[108:111], v[4:5], off offset:96
	global_load_dwordx4 v[112:115], v[4:5], off offset:128
	global_load_dwordx4 v[116:119], v[4:5], off offset:160
	global_load_dwordx4 v[120:123], v[4:5], off offset:192
	global_load_dwordx4 v[124:127], v[4:5], off offset:224
	global_load_dwordx4 v[26:29], v[4:5], off offset:256
	global_load_dwordx4 v[0:3], v[4:5], off offset:288
	global_load_dwordx4 v[30:33], v[4:5], off offset:320
	s_nop 0
	global_load_dwordx4 v[4:7], v[4:5], off offset:352
	s_waitcnt vmcnt(24)
	v_lshlrev_b32_e32 v13, 4, v11
	global_load_dwordx2 v[14:15], v[8:9], off
	v_readfirstlane_b32 s0, v156
	s_ashr_i32 s5, s4, 31
	s_lshl_b32 s2, s0, 10
	s_lshl_b64 s[0:1], s[4:5], 12
	s_add_u32 s0, s26, s0
	s_addc_u32 s1, s27, s1
	s_add_i32 s29, s2, 0
	s_mov_b32 m0, s29
	s_add_i32 s2, s29, 0xc000
	v_and_b32_e32 v10, 63, v11
	v_and_b32_e32 v12, 0xc0, v13
	v_mov_b32_e32 v151, v193
	v_lshlrev_b32_e32 v145, 8, v154
	v_lshlrev_b32_e32 v167, 7, v154
	v_lshl_add_u32 v163, v154, 2, v157
	v_mov_b32_e32 v174, 0
	v_mov_b32_e32 v173, 0xf149f2ca
	s_waitcnt vmcnt(4)
	v_lshlrev_b32_e32 v17, 16, v26
	s_waitcnt vmcnt(2)
	v_lshlrev_b32_e32 v16, 16, v30
	s_waitcnt vmcnt(0)
	v_pk_mul_f32 v[18:19], v[14:15], v[16:17] op_sel:[0,1] op_sel_hi:[1,0]
	v_pk_mul_f32 v[14:15], v[14:15], v[16:17]
	v_sub_f32_e32 v18, v18, v19
	v_add_f32_e32 v14, v15, v14
	v_cvt_pk_bf16_f32 v15, v18, v193
	v_cvt_pk_bf16_f32 v14, v14, v193
	global_load_dwordx2 v[16:17], v[8:9], off offset:8
	v_and_b32_e32 v19, 0xffff0000, v26
	v_and_b32_e32 v18, 0xffff0000, v30
	s_waitcnt vmcnt(0)
	v_pk_mul_f32 v[20:21], v[16:17], v[18:19] op_sel:[0,1] op_sel_hi:[1,0]
	v_pk_mul_f32 v[16:17], v[16:17], v[18:19]
	v_sub_f32_e32 v20, v20, v21
	v_add_f32_e32 v16, v16, v17
	v_cvt_pk_bf16_f32 v17, v20, v193
	v_cvt_pk_bf16_f32 v16, v16, v193
	global_load_dwordx2 v[18:19], v[8:9], off offset:16
	v_lshlrev_b32_e32 v21, 16, v27
	v_lshlrev_b32_e32 v20, 16, v31
	s_waitcnt vmcnt(0)
	v_pk_mul_f32 v[22:23], v[18:19], v[20:21] op_sel:[0,1] op_sel_hi:[1,0]
	v_pk_mul_f32 v[18:19], v[18:19], v[20:21]
	v_sub_f32_e32 v22, v22, v23
	v_add_f32_e32 v18, v18, v19
	v_cvt_pk_bf16_f32 v19, v22, v193
	v_cvt_pk_bf16_f32 v18, v18, v193
	global_load_dwordx2 v[20:21], v[8:9], off offset:24
	v_and_b32_e32 v23, 0xffff0000, v27
	v_and_b32_e32 v22, 0xffff0000, v31
	s_waitcnt vmcnt(0)
	v_pk_mul_f32 v[24:25], v[20:21], v[22:23] op_sel:[0,1] op_sel_hi:[1,0]
	v_pk_mul_f32 v[20:21], v[20:21], v[22:23]
	v_sub_f32_e32 v24, v24, v25
	v_add_f32_e32 v20, v20, v21
	v_cvt_pk_bf16_f32 v21, v24, v193
	v_cvt_pk_bf16_f32 v20, v20, v193
	global_load_dwordx2 v[22:23], v[8:9], off offset:32
	v_lshlrev_b32_e32 v25, 16, v28
	v_lshlrev_b32_e32 v24, 16, v32
	s_waitcnt vmcnt(0)
	v_pk_mul_f32 v[26:27], v[22:23], v[24:25] op_sel:[0,1] op_sel_hi:[1,0]
	v_pk_mul_f32 v[22:23], v[22:23], v[24:25]
	v_sub_f32_e32 v26, v26, v27
	v_add_f32_e32 v22, v22, v23
	v_cvt_pk_bf16_f32 v23, v26, v193
	v_cvt_pk_bf16_f32 v22, v22, v193
	global_load_dwordx2 v[24:25], v[8:9], off offset:40
	v_and_b32_e32 v27, 0xffff0000, v28
	v_and_b32_e32 v26, 0xffff0000, v32
	s_waitcnt vmcnt(0)
	v_pk_mul_f32 v[30:31], v[24:25], v[26:27] op_sel:[0,1] op_sel_hi:[1,0]
	v_pk_mul_f32 v[24:25], v[24:25], v[26:27]
	v_sub_f32_e32 v28, v30, v31
	v_add_f32_e32 v24, v24, v25
	v_cvt_pk_bf16_f32 v25, v28, v193
	v_cvt_pk_bf16_f32 v24, v24, v193
	global_load_dwordx2 v[26:27], v[8:9], off offset:48
	v_lshlrev_b32_e32 v31, 16, v29
	v_lshlrev_b32_e32 v30, 16, v33
	v_and_b32_e32 v29, 0xffff0000, v29
	s_waitcnt vmcnt(0)
; __device__ __forceinline__ unsigned cvt_pk_bf16(float lo, float hi) { unsigned r; asm volatile("v_cvt_pk_bf16_f32 %0, %1, %2" : "=v"(r) : "v"(lo), "v"(hi)); return r; }
;     ...
;             const f32x2* rt = P.ropeM + (size_t)(qrow & (SEQ - 1)) * 32;
; #pragma unroll
;             for (int g = 0; g < 2; ++g) {
;                 bf16x8 x1 = qr[8 + g], x2 = qr[10 + g];
; #pragma unroll
;                 for (int e = 0; e < 8; ++e) { const f32x2 cs = rt[g * 16 + hi * 8 + e];
;                     const float a = bf2f((unsigned short)x1[e]), c = bf2f((unsigned short)x2[e]);
;                     const float ra = a * cs.x - c * cs.y, rc = c * cs.x + a * cs.y;
;                     x1[e] = (short)(cvt_pk_bf16(ra, 0.f) & 0xffffu); x2[e] = (short)(cvt_pk_bf16(rc, 0.f) & 0xffffu); }
;                 qr[8 + g] = x1; qr[10 + g] = x2;
;             }
	v_pk_mul_f32 v[34:35], v[26:27], v[30:31] op_sel:[0,1] op_sel_hi:[1,0]
	v_pk_mul_f32 v[26:27], v[26:27], v[30:31]
	v_sub_f32_e32 v28, v34, v35
	v_add_f32_e32 v26, v26, v27
	v_cvt_pk_bf16_f32 v27, v28, v193
	v_cvt_pk_bf16_f32 v26, v26, v193
	global_load_dwordx2 v[30:31], v[8:9], off offset:56
	v_and_b32_e32 v28, 0xffff0000, v33
	v_lshlrev_b32_e32 v35, 16, v0
	v_lshlrev_b32_e32 v34, 16, v4
	s_waitcnt vmcnt(0)
	v_pk_mul_f32 v[32:33], v[30:31], v[28:29] op_sel:[0,1] op_sel_hi:[1,0]
	v_pk_mul_f32 v[28:29], v[30:31], v[28:29]
	v_sub_f32_e32 v32, v32, v33
	v_add_f32_e32 v28, v28, v29
	v_cvt_pk_bf16_f32 v30, v32, v193
	v_cvt_pk_bf16_f32 v28, v28, v193
	global_load_dwordx2 v[32:33], v[8:9], off offset:128
	s_waitcnt vmcnt(0)
	v_pk_mul_f32 v[36:37], v[32:33], v[34:35] op_sel:[0,1] op_sel_hi:[1,0]
	v_pk_mul_f32 v[32:33], v[32:33], v[34:35]
	v_sub_f32_e32 v29, v36, v37
	v_add_f32_e32 v32, v32, v33
	v_cvt_pk_bf16_f32 v31, v29, v193
	v_cvt_pk_bf16_f32 v29, v32, v193
	global_load_dwordx2 v[32:33], v[8:9], off offset:136
	v_and_b32_e32 v35, 0xffff0000, v0
	v_and_b32_e32 v34, 0xffff0000, v4
	s_waitcnt vmcnt(0)
	v_pk_mul_f32 v[36:37], v[32:33], v[34:35] op_sel:[0,1] op_sel_hi:[1,0]
	v_pk_mul_f32 v[32:33], v[32:33], v[34:35]
	v_sub_f32_e32 v0, v36, v37
	v_add_f32_e32 v4, v32, v33
	v_cvt_pk_bf16_f32 v32, v0, v193
	v_cvt_pk_bf16_f32 v4, v4, v193
	global_load_dwordx2 v[34:35], v[8:9], off offset:144
	v_lshlrev_b32_e32 v37, 16, v1
	v_lshlrev_b32_e32 v36, 16, v5
	v_and_b32_e32 v1, 0xffff0000, v1
	s_waitcnt vmcnt(0)
	v_pk_mul_f32 v[38:39], v[34:35], v[36:37] op_sel:[0,1] op_sel_hi:[1,0]
	v_pk_mul_f32 v[34:35], v[34:35], v[36:37]
	v_sub_f32_e32 v0, v38, v39
	v_add_f32_e32 v33, v34, v35
	v_cvt_pk_bf16_f32 v34, v0, v193
	v_cvt_pk_bf16_f32 v33, v33, v193
	global_load_dwordx2 v[36:37], v[8:9], off offset:152
	v_and_b32_e32 v0, 0xffff0000, v5
	s_waitcnt vmcnt(0)
	v_pk_mul_f32 v[38:39], v[36:37], v[0:1] op_sel:[0,1] op_sel_hi:[1,0]
	v_pk_mul_f32 v[0:1], v[36:37], v[0:1]
	v_sub_f32_e32 v5, v38, v39
	v_add_f32_e32 v0, v0, v1
	v_cvt_pk_bf16_f32 v35, v5, v193
	v_cvt_pk_bf16_f32 v5, v0, v193
	global_load_dwordx2 v[0:1], v[8:9], off offset:160
	v_lshlrev_b32_e32 v37, 16, v2
	v_lshlrev_b32_e32 v36, 16, v6
	s_waitcnt vmcnt(0)
	v_pk_mul_f32 v[38:39], v[0:1], v[36:37] op_sel:[0,1] op_sel_hi:[1,0]
	v_pk_mul_f32 v[0:1], v[0:1], v[36:37]
	v_sub_f32_e32 v38, v38, v39
	v_add_f32_e32 v0, v0, v1
	v_cvt_pk_bf16_f32 v37, v38, v193
	v_cvt_pk_bf16_f32 v36, v0, v193
	global_load_dwordx2 v[0:1], v[8:9], off offset:168
	v_and_b32_e32 v39, 0xffff0000, v2
	v_and_b32_e32 v38, 0xffff0000, v6
	s_waitcnt vmcnt(0)
	v_pk_mul_f32 v[40:41], v[0:1], v[38:39] op_sel:[0,1] op_sel_hi:[1,0]
	v_pk_mul_f32 v[0:1], v[0:1], v[38:39]
	v_sub_f32_e32 v2, v40, v41
	v_add_f32_e32 v0, v0, v1
	v_cvt_pk_bf16_f32 v6, v2, v193
	v_cvt_pk_bf16_f32 v2, v0, v193
	global_load_dwordx2 v[0:1], v[8:9], off offset:176
	v_lshlrev_b32_e32 v39, 16, v3
	v_lshlrev_b32_e32 v38, 16, v7
	s_waitcnt vmcnt(0)
	v_pk_mul_f32 v[40:41], v[0:1], v[38:39] op_sel:[0,1] op_sel_hi:[1,0]
	v_pk_mul_f32 v[0:1], v[0:1], v[38:39]
	v_sub_f32_e32 v40, v40, v41
	v_add_f32_e32 v0, v0, v1
	v_cvt_pk_bf16_f32 v39, v40, v193
	v_cvt_pk_bf16_f32 v38, v0, v193
	global_load_dwordx2 v[0:1], v[8:9], off offset:184
	v_and_b32_e32 v9, 0xffff0000, v3
	v_and_b32_e32 v8, 0xffff0000, v7
	s_waitcnt vmcnt(0)
; #define VM_WAIT() asm volatile("s_waitcnt vmcnt(0)" ::: "memory")
;     ...
;         } else if constexpr (ATT_GLDS) {
;         unsigned gsv[2], gsk[2], gsk2 = 0u;
; #pragma unroll
;         for (int i = 0; i < 2; ++i) { const int a = (i * 512 + tid) * 16;
;             { const int sub = a >> 9, within = a & 511; const int kk = (sub >> 2) * 8 + (within >> 6); const int k = (kk & ~0xC) | ((kk & 4) << 1) | ((kk & 8) >> 1);
;               const int c = (sub & 3) * 32 + ((within & 63) >> 1); gsv[i] = (unsigned)(k * ldv + c) * 2u; }
;             if constexpr (MODE == MODE_DIFF) { if (i == 0) { const int row = a >> 7, ch = ((a >> 4) & 7) ^ ((row >> 1) & 7); gsk[0] = (unsigned)(row * ldk + ch * 8) * 2u; } gsk[1] = 0u; }
;             else { const int row = a >> 8, ch = ((a >> 4) & 15) ^ (row & 15); gsk[i] = (unsigned)(row * ldk + ch * 8) * 2u; } }
;         if constexpr (MODE == MODE_MLA) { const int a = tid * 16, row = a >> 7, ch = ((a >> 4) & 7) ^ ((row >> 1) & 7); gsk2 = (unsigned)(row * UW + ch * 8) * 2u; }
;         const unsigned ldsw = (unsigned)__builtin_amdgcn_readfirstlane(wid) * 1024u;
;     ...
;         GLDS(0, 0); VM_WAIT(); __syncthreads();
; #pragma unroll 1
;         for (int t = 0; t < NT; ++t) {
	v_pk_mul_f32 v[40:41], v[0:1], v[8:9] op_sel:[0,1] op_sel_hi:[1,0]
	v_pk_mul_f32 v[0:1], v[0:1], v[8:9]
	v_sub_f32_e32 v3, v40, v41
	v_add_f32_e32 v0, v0, v1
	v_bfe_i32 v9, v11, 4, 24
	v_cvt_pk_bf16_f32 v8, v3, v193
	v_cvt_pk_bf16_f32 v7, v0, v193
	v_bfe_u32 v0, v11, 2, 2
	v_lshrrev_b32_e32 v1, 1, v11
	v_lshlrev_b32_e32 v3, 1, v11
	v_lshrrev_b32_e32 v41, 1, v9
	v_and_or_b32 v0, v1, 8, v0
	v_and_b32_e32 v1, 0xc0, v3
	v_and_b32_e32 v40, 0xffff0, v9
	v_and_b32_e32 v41, 4, v41
	v_and_or_b32 v1, v13, 48, v1
	v_or3_b32 v40, v40, v41, v0
	v_lshl_or_b32 v192, v40, 12, v1
	v_xor_b32_e32 v40, v9, v11
	v_lshlrev_b32_e32 v9, 12, v9
	v_lshlrev_b32_e32 v40, 4, v40
	v_and_or_b32 v146, v40, s87, v9
	v_add_u32_e32 v9, 0x2000, v13
	v_ashrrev_i32_e32 v9, 8, v9
	v_lshrrev_b32_e32 v41, 1, v9
	v_and_b32_e32 v40, 0xffff0, v9
	v_and_b32_e32 v41, 4, v41
	v_or3_b32 v0, v40, v41, v0
	v_lshl_add_u64 v[40:41], s[0:1], 0, v[192:193]
	v_lshl_or_b32 v148, v0, 12, v1
	v_lshl_add_u64 v[40:41], v[40:41], 0, s[36:37]
	global_load_lds_dwordx4 v[40:41], off
	v_lshl_add_u64 v[40:41], s[0:1], 0, v[148:149]
	v_xor_b32_e32 v0, v9, v11
	v_lshl_add_u64 v[40:41], v[40:41], 0, s[36:37]
	s_add_i32 m0, s29, 0x2000
	v_lshlrev_b32_e32 v1, 12, v9
	v_lshlrev_b32_e32 v0, 4, v0
	global_load_lds_dwordx4 v[40:41], off
	s_mov_b32 m0, s2
	v_and_or_b32 v150, v0, s87, v1
	global_load_lds_dwordx4 v146, s[0:1]
	s_add_i32 m0, s29, 0xe000
	v_lshlrev_b32_e32 v0, 10, v11
	global_load_lds_dwordx4 v150, s[0:1]
	s_lshl_b64 s[0:1], s[4:5], 13
	v_and_b32_e32 v0, 0xffffe000, v0
	v_xor_b32_e32 v1, v13, v11
	s_add_u32 s0, s14, s0
	v_and_or_b32 v0, v1, s3, v0
	s_addc_u32 s1, s15, s1
	s_add_i32 m0, s29, 0x10000
	v_mov_b32_e32 v1, v193
	global_load_lds_dwordx4 v0, s[0:1]
	v_lshl_add_u64 v[152:153], s[14:15], 0, v[0:1]
	v_bitop3_b32 v0, v155, v11, 15 bitop3:0x78
	v_lshlrev_b32_e32 v9, 3, v11
	v_lshlrev_b32_e32 v158, 4, v0
	v_and_b32_e32 v0, 0xf0, v13
	v_bitop3_b32 v159, v144, v0, 32 bitop3:0x36
	v_bitop3_b32 v160, v144, v0, 64 bitop3:0x36
	v_bitop3_b32 v161, v144, v0, s60 bitop3:0x36
	v_bitop3_b32 v162, v144, v0, s59 bitop3:0x36
	v_bitop3_b32 v164, v144, v0, s61 bitop3:0x36
	v_bitop3_b32 v165, v144, v0, s58 bitop3:0x36
	v_bitop3_b32 v166, v144, v0, s62 bitop3:0x36
	v_and_b32_e32 v0, 0x70, v9
	v_bitop3_b32 v169, v144, v0, 32 bitop3:0x36
	v_bitop3_b32 v170, v144, v0, 64 bitop3:0x36
	v_bitop3_b32 v171, v144, v0, s60 bitop3:0x36
	v_and_b32_e32 v0, 0x118, v9
	s_mov_b32 s0, 0x5040100
	s_waitcnt vmcnt(0)
	v_perm_b32 v128, v17, v15, s0
	v_perm_b32 v136, v16, v14, s0
	v_and_or_b32 v0, v3, 32, v0
	v_mov_b32_e32 v14, v193
	v_mov_b32_e32 v15, v193
	v_bitop3_b32 v168, v144, v9, s3 bitop3:0x78
	v_cmp_gt_u32_e64 s[2:3], 32, v10
	v_perm_b32 v129, v21, v19, s0
	v_perm_b32 v130, v25, v23, s0
	v_perm_b32 v131, v30, v27, s0
	v_perm_b32 v132, v32, v31, s0
	v_perm_b32 v133, v35, v34, s0
	v_perm_b32 v134, v6, v37, s0
	v_perm_b32 v135, v8, v39, s0
	v_perm_b32 v137, v20, v18, s0
	v_perm_b32 v138, v24, v22, s0
	v_perm_b32 v139, v28, v26, s0
	v_perm_b32 v140, v4, v29, s0
	v_perm_b32 v141, v5, v33, s0
	v_perm_b32 v142, v2, v36, s0
	v_perm_b32 v143, v7, v38, s0
	v_add3_u32 v172, v12, 0, v0
	v_mov_b32_e32 v0, v193
	v_mov_b32_e32 v2, v193
	v_mov_b32_e32 v3, v193
	v_mov_b32_e32 v4, v193
	v_mov_b32_e32 v5, v193
	v_mov_b32_e32 v6, v193
	v_mov_b32_e32 v7, v193
	v_mov_b32_e32 v8, v193
	v_mov_b32_e32 v9, v193
	v_mov_b32_e32 v10, v193
	v_mov_b32_e32 v11, v193
	v_mov_b32_e32 v12, v193
	v_mov_b32_e32 v13, v193
	v_mov_b64_e32 v[30:31], v[14:15]
	v_mov_b64_e32 v[46:47], v[14:15]
	v_mov_b64_e32 v[62:63], v[14:15]
	s_or_b32 s16, s4, 64
	v_mov_b64_e32 v[28:29], v[12:13]
	v_mov_b64_e32 v[26:27], v[10:11]
	v_mov_b64_e32 v[24:25], v[8:9]
	v_mov_b64_e32 v[22:23], v[6:7]
	v_mov_b64_e32 v[20:21], v[4:5]
	v_mov_b64_e32 v[18:19], v[2:3]
	v_mov_b64_e32 v[16:17], v[0:1]
	v_mov_b64_e32 v[44:45], v[12:13]
	v_mov_b64_e32 v[42:43], v[10:11]
	v_mov_b64_e32 v[40:41], v[8:9]
	v_mov_b64_e32 v[38:39], v[6:7]
	v_mov_b64_e32 v[36:37], v[4:5]
	v_mov_b64_e32 v[34:35], v[2:3]
	v_mov_b64_e32 v[32:33], v[0:1]
	v_mov_b64_e32 v[60:61], v[12:13]
	v_mov_b64_e32 v[58:59], v[10:11]
	v_mov_b64_e32 v[56:57], v[8:9]
	v_mov_b64_e32 v[54:55], v[6:7]
	v_mov_b64_e32 v[52:53], v[4:5]
	v_mov_b64_e32 v[50:51], v[2:3]
	v_mov_b64_e32 v[48:49], v[0:1]
	s_waitcnt vmcnt(0) lgkmcnt(0)
	s_barrier
	s_and_b32 s30, s28, 1
	s_cmp_eq_u32 s28, 63
	s_cbranch_scc1 .LBB0_788
	s_branch .LBB0_787

;     __device__ __forceinline__ const float* in(int i) const { return *(const float* const __attribute__((address_space(4)))*)(p + 8 * i); }
;     __device__ __forceinline__ unsigned char* ws() const { return *(unsigned char* const __attribute__((address_space(4)))*)(p + 232); }
; __device__ __forceinline__ CvtDesc conv_expert_desc(const KA& a, unsigned char* ws, int q) {
;     const int l = q / Q_PER_L; int r = q - l * Q_PER_L;
;     unsigned char* wl = ws + WS_W + (size_t)l * W_LSTRIDE;
;     CvtDesc d; d.f8 = (MOE_FP8_LAST && (MOE_FP8_GU_ALL || l == NLAYER - 1)) ? 1 : 0;
;     if (MOE_FP8_LAST && MOE_FP8_DOWN_ALL && r >= 2 * Q_IG) d.f8 = 1;
;     const int eb = d.f8 ? 1 : 2;
;     if (r < 2 * Q_IG) { const int up = r >= Q_IG; if (up) r -= Q_IG; const int e = r >> 8, rr = r & 255, kb = rr >> 3, nb = rr & 7, n0 = nb * 64;
;         const float* src = e < 64 ? a.in(up ? 21 : 20) + ((size_t)l * 64 + e) * DM * FFE : a.in(up ? 24 : 23) + (size_t)l * DM * FFE;
;         d.src = src + (size_t)(kb * 64) * FFE + n0; d.N = FFE; d.dKB = DM * eb;
;         d.dst = wl + W_GU + ((size_t)e * 1024 * DM + (size_t)((n0 >> 7) * 256 + up * 128 + (n0 & 127)) * DM + kb * 64) * eb;
;     } else { r -= 2 * Q_IG; const int e = r >> 8, rr = r & 255, kb = rr >> 5, nb = rr & 31;
;         const float* src = e < 64 ? a.in(22) + ((size_t)l * 64 + e) * FFE * DM : a.in(25) + (size_t)l * FFE * DM;
;         d.src = src + (size_t)(kb * 64) * DM + nb * 64; d.N = DM; d.dKB = FFE * eb;
;         d.dst = wl + W_D + ((size_t)e * DM * FFE + (size_t)(nb * 64) * FFE + kb * 64) * eb; }
;     return d;
.LBB0_788:
	s_add_u32 s52, s52, 31
	s_cmp_ge_u32 s52, 62
	s_cselect_b32 s50, 1, 0
	s_cbranch_scc0 .Lilc_n_m
	s_sub_u32 s52, s52, 62
	s_mov_b32 s46, s51
	s_add_u32 s51, s51, 1
	s_lshl_b32 s49, s46, 2
	s_add_u32 s49, s49, s54
	s_cmp_lt_u32 s49, 0xc3
	s_cselect_b32 s50, 1, 0
	s_cbranch_scc0 .Lilc_n_m
	s_lshr_b32 s55, s46, 4
	s_and_b32 s57, s49, 63
	s_lshl_b32 s101, s56, 6
	s_add_u32 s101, s101, s57
	s_cmp_eq_u32 s55, 3
	s_cselect_b32 s55, s54, s55
	s_cselect_b32 s100, 3, 0
	s_cselect_b32 s101, s56, s101
	s_cselect_b32 s57, 64, s57
	s_add_u32 s100, s100, s55
	s_lshl_b32 s100, s100, 3
	s_add_u32 s100, s100, 0xa0
	s_load_dwordx2 s[44:45], s[6:7], s100
